# indexer step 1: f16 order-preserving keys of 12 of 16 scores per tile built with packed 16-bit ops (cvt_pk, pk_ashr, bitop3): 8 instead of 17 VALU per key pair, identical keys; on top of sparse saddr
# speedup vs baseline: 1.0100x; 1.0100x over previous
_Z6mk_fwd4Args:
	s_mov_b32 s32, 0x80008000
	s_load_dword s3, s[0:1], 0xb0
	s_add_u32 s4, s0, 0xb0
	v_lshl_add_u32 v1, v0, 2, 0
	v_add_u32_e32 v1, 0x20000, v1
	v_mov_b32_e32 v2, 0
	s_waitcnt lgkmcnt(0)
	v_writelane_b32 v254, s3, 0
	v_writelane_b32 v254, s0, 1
	s_addc_u32 s5, s1, 0
	ds_write2st64_b32 v1, v2, v2 offset1:8
	ds_write2st64_b32 v1, v2, v2 offset0:16 offset1:24
	v_writelane_b32 v254, s1, 2
	v_writelane_b32 v254, s4, 3
	v_or_b32_e32 v1, 0x800, v0
	s_mov_b64 s[0:1], -1
	v_writelane_b32 v254, s5, 4
	s_and_saveexec_b64 s[4:5], s[0:1]
	v_lshl_add_u32 v3, v1, 2, 0
	v_add_u32_e32 v3, 0x20000, v3
	ds_write_b32 v3, v2
	s_or_b64 exec, exec, s[4:5]
	s_and_saveexec_b64 s[4:5], s[0:1]
	s_add_i32 s0, 0, 0x20000
	v_lshl_add_u32 v1, v1, 2, s0
	v_mov_b32_e32 v2, 0
	ds_write_b32 v1, v2 offset:2048
	s_or_b64 exec, exec, s[4:5]
	v_or_b32_e32 v1, 0xc00, v0
	v_cmp_gt_u32_e64 s[0:1], 7, 6
	v_cmp_gt_u32_e64 s[6:7], 7, 5
	s_and_saveexec_b64 s[4:5], s[6:7]
	v_lshl_add_u32 v2, v1, 2, 0
	v_add_u32_e32 v2, 0x20000, v2
	v_mov_b32_e32 v3, 0
	ds_write_b32 v2, v3
	s_or_b64 exec, exec, s[4:5]
	v_readlane_b32 s4, v254, 1
	v_readlane_b32 s5, v254, 2
	s_load_dwordx2 s[64:65], s[4:5], 0xa0
	s_and_saveexec_b64 s[4:5], s[0:1]
	s_add_i32 s0, 0, 0x20000
	v_lshl_add_u32 v1, v1, 2, s0
	v_mov_b32_e32 v2, 0
	ds_write_b32 v1, v2 offset:2048
	s_mov_b32 s62, s2
	s_or_b64 exec, exec, s[4:5]
	s_waitcnt lgkmcnt(0)
	s_barrier
	s_getreg_b32 s3, hwreg(HW_REG_XCC_ID, 0, 4)
	v_cmp_eq_u32_e64 s[4:5], 0, v0
	s_mov_b64 s[0:1], exec
	s_nop 0
	v_writelane_b32 v254, s4, 5
	s_nop 1
	v_writelane_b32 v254, s5, 6
	s_and_b64 s[4:5], s[0:1], s[4:5]
	s_mov_b64 exec, s[4:5]
	s_cbranch_execz .LBB0_11
	s_mov_b64 s[4:5], exec
	v_mbcnt_lo_u32_b32 v1, s4, 0
	v_mbcnt_hi_u32_b32 v1, s5, v1
	v_cmp_eq_u32_e32 vcc, 0, v1
	s_and_b64 s[6:7], exec, vcc
	s_mov_b64 exec, s[6:7]
	s_cbranch_execz .LBB0_11
	s_lshl_b32 s3, s3, 8
	s_and_b32 s3, s3, 0xf00
	s_add_u32 s6, s64, s3
	s_addc_u32 s7, s65, 0
	s_bcnt1_i32_b64 s3, s[4:5]
	v_mov_b32_e32 v1, 0x39801000
	v_mov_b32_e32 v2, s3
	global_atomic_add v1, v2, s[6:7] offset:1024

.LBB0_382:
	ds_read_b128 v[4:7], v214
	ds_read_b128 v[26:29], v214 offset:1024
	s_cmp_eq_u32 s81, s0
	s_mov_b64 s[0:1], -1
	s_waitcnt lgkmcnt(1)
	v_mfma_f32_32x32x16_bf16 v[10:25], v[80:83], v[4:7], 0
	ds_read_b128 v[4:7], v214 offset:2048
	ds_read_b128 v[30:33], v214 offset:3072
	s_waitcnt lgkmcnt(2)
	v_mfma_f32_32x32x16_bf16 v[10:25], v[76:79], v[26:29], v[10:25]
	s_waitcnt lgkmcnt(1)
	v_mfma_f32_32x32x16_bf16 v[10:25], v[72:75], v[4:7], v[10:25]
	s_waitcnt lgkmcnt(0)
	v_mfma_f32_32x32x16_bf16 v[10:25], v[52:55], v[30:33], v[10:25]
	ds_read_b128 v[26:29], v214 offset:7168
	ds_read_b128 v[30:33], v214 offset:6144
	ds_read_b128 v[34:37], v214 offset:5120
	ds_read_b128 v[4:7], v214 offset:4096
	s_nop 7
	v_fma_f32 v48, |v10|, v2, 0
	v_fma_f32 v49, |v11|, v2, 0
	v_fma_f32 v50, |v12|, v2, 0
	v_fma_f32 v51, |v13|, v2, 0
	v_fma_f32 v212, |v14|, v2, 0
	v_fma_f32 v213, |v15|, v2, 0
	v_fma_f32 v215, |v16|, v2, 0
	v_fma_f32 v216, |v17|, v2, 0
	v_fma_f32 v217, |v18|, v2, 0
	v_fma_f32 v228, |v19|, v2, 0
	s_waitcnt lgkmcnt(0)
	v_mfma_f32_32x32x16_bf16 v[4:19], v[80:83], v[4:7], 0
	v_fma_f32 v229, |v20|, v2, 0
	v_fma_f32 v230, |v21|, v2, 0
	v_mfma_f32_32x32x16_bf16 v[4:19], v[76:79], v[34:37], v[4:19]
	v_fma_f32 v234, |v22|, v2, 0
	v_fma_f32 v235, |v23|, v2, 0
	v_mfma_f32_32x32x16_bf16 v[4:19], v[72:75], v[30:33], v[4:19]
	v_fma_f32 v236, |v24|, v2, 0
	v_fma_f32 v237, |v25|, v2, 0
	v_mfma_f32_32x32x16_bf16 v[4:19], v[52:55], v[26:29], v[4:19]
	ds_read_b128 v[20:23], v214 offset:8192
	ds_read_b128 v[36:39], v214 offset:9216
	ds_read_b128 v[40:43], v214 offset:10240
	ds_read_b128 v[44:47], v214 offset:11264
	s_nop 7
	v_fma_f32 v48, |v4|, v249, v48
	s_waitcnt lgkmcnt(3)
	v_mfma_f32_32x32x16_bf16 v[20:35], v[80:83], v[20:23], 0
	v_fma_f32 v49, |v5|, v249, v49
	v_fma_f32 v50, |v6|, v249, v50
	v_fma_f32 v51, |v7|, v249, v51
	s_waitcnt lgkmcnt(2)
	v_mfma_f32_32x32x16_bf16 v[20:35], v[76:79], v[36:39], v[20:35]
	v_fma_f32 v8, |v8|, v249, v212
	v_fma_f32 v9, |v9|, v249, v213
	v_fma_f32 v10, |v10|, v249, v215
	v_fma_f32 v11, |v11|, v249, v216
	s_waitcnt lgkmcnt(1)
	v_mfma_f32_32x32x16_bf16 v[20:35], v[72:75], v[40:43], v[20:35]
	v_fma_f32 v12, |v12|, v249, v217
	v_fma_f32 v13, |v13|, v249, v228
	v_fma_f32 v212, |v14|, v249, v229
	v_fma_f32 v213, |v15|, v249, v230
	v_fma_f32 v215, |v16|, v249, v234
	v_fma_f32 v216, |v17|, v249, v235
	v_fma_f32 v217, |v18|, v249, v236
	v_fma_f32 v228, |v19|, v249, v237
	s_waitcnt lgkmcnt(0)
	v_mfma_f32_32x32x16_bf16 v[20:35], v[52:55], v[44:47], v[20:35]
	ds_read_b128 v[4:7], v214 offset:12288
	ds_read_b128 v[36:39], v214 offset:13312
	ds_read_b128 v[40:43], v214 offset:14336
	ds_read_b128 v[44:47], v214 offset:15360
	s_nop 7
	v_fma_f32 v24, |v24|, v250, v8
	v_fma_f32 v25, |v25|, v250, v9
	v_fma_f32 v26, |v26|, v250, v10
	v_fma_f32 v27, |v27|, v250, v11
	v_fma_f32 v28, |v28|, v250, v12
	v_fma_f32 v29, |v29|, v250, v13
	s_waitcnt lgkmcnt(3)
	v_mfma_f32_32x32x16_bf16 v[4:19], v[80:83], v[4:7], 0
	v_fma_f32 v48, |v20|, v250, v48
	v_fma_f32 v49, |v21|, v250, v49
	v_fma_f32 v50, |v22|, v250, v50
	v_fma_f32 v51, |v23|, v250, v51
	s_waitcnt lgkmcnt(2)
	v_mfma_f32_32x32x16_bf16 v[4:19], v[76:79], v[36:39], v[4:19]
	v_fma_f32 v212, |v30|, v250, v212
	s_waitcnt lgkmcnt(1)
	v_mfma_f32_32x32x16_bf16 v[4:19], v[72:75], v[40:43], v[4:19]
	v_fma_f32 v213, |v31|, v250, v213
	v_fma_f32 v215, |v32|, v250, v215
	v_fma_f32 v216, |v33|, v250, v216
	v_fma_f32 v217, |v34|, v250, v217
	v_fma_f32 v228, |v35|, v250, v228
	s_waitcnt lgkmcnt(0)
	v_mfma_f32_32x32x16_bf16 v[4:19], v[52:55], v[44:47], v[4:19]
	ds_read_b128 v[20:23], v214 offset:16384
	ds_read_b128 v[36:39], v214 offset:17408
	ds_read_b128 v[40:43], v214 offset:18432
	ds_read_b128 v[44:47], v214 offset:19456
	s_nop 7
	v_fma_f32 v229, |v8|, v251, v24
	v_fma_f32 v230, |v9|, v251, v25
	v_fma_f32 v234, |v10|, v251, v26
	v_fma_f32 v235, |v11|, v251, v27
	v_fma_f32 v236, |v12|, v251, v28
	v_fma_f32 v237, |v13|, v251, v29
	s_waitcnt lgkmcnt(3)
	v_mfma_f32_32x32x16_bf16 v[20:35], v[80:83], v[20:23], 0
	v_fma_f32 v48, |v4|, v251, v48
	v_fma_f32 v49, |v5|, v251, v49
	v_fma_f32 v50, |v6|, v251, v50
	v_fma_f32 v51, |v7|, v251, v51
	s_waitcnt lgkmcnt(2)
	v_mfma_f32_32x32x16_bf16 v[20:35], v[76:79], v[36:39], v[20:35]
	v_fma_f32 v212, |v14|, v251, v212
	s_waitcnt lgkmcnt(1)
	v_mfma_f32_32x32x16_bf16 v[20:35], v[72:75], v[40:43], v[20:35]
	v_fma_f32 v213, |v15|, v251, v213
	v_fma_f32 v215, |v16|, v251, v215
	v_fma_f32 v216, |v17|, v251, v216
	v_fma_f32 v217, |v18|, v251, v217
	v_fma_f32 v228, |v19|, v251, v228
	s_waitcnt lgkmcnt(0)
	v_mfma_f32_32x32x16_bf16 v[20:35], v[52:55], v[44:47], v[20:35]
	ds_read_b128 v[4:7], v214 offset:20480
	ds_read_b128 v[8:11], v214 offset:21504
	ds_read_b128 v[12:15], v214 offset:22528
	ds_read_b128 v[16:19], v214 offset:23552
	s_nop 7
	v_fma_f32 v20, |v20|, v252, v48
	v_fma_f32 v21, |v21|, v252, v49
	v_fma_f32 v22, |v22|, v252, v50
	v_fma_f32 v23, |v23|, v252, v51
	s_waitcnt lgkmcnt(3)
	v_mfma_f32_32x32x16_bf16 v[36:51], v[80:83], v[4:7], 0
	v_fma_f32 v24, |v24|, v252, v229
	v_fma_f32 v25, |v25|, v252, v230
	s_waitcnt lgkmcnt(2)
	v_mfma_f32_32x32x16_bf16 v[36:51], v[76:79], v[8:11], v[36:51]
	v_fma_f32 v26, |v26|, v252, v234
	v_fma_f32 v27, |v27|, v252, v235
	s_waitcnt lgkmcnt(1)
	v_mfma_f32_32x32x16_bf16 v[36:51], v[72:75], v[12:15], v[36:51]
	v_fma_f32 v229, |v28|, v252, v236
	v_fma_f32 v230, |v29|, v252, v237
	v_fma_f32 v212, |v30|, v252, v212
	v_fma_f32 v213, |v31|, v252, v213
	v_fma_f32 v215, |v32|, v252, v215
	v_fma_f32 v216, |v33|, v252, v216
	v_fma_f32 v217, |v34|, v252, v217
	v_fma_f32 v228, |v35|, v252, v228
	s_waitcnt lgkmcnt(0)
	v_mfma_f32_32x32x16_bf16 v[36:51], v[52:55], v[16:19], v[36:51]
	ds_read_b128 v[4:7], v214 offset:24576
	ds_read_b128 v[8:11], v214 offset:25600
	ds_read_b128 v[28:31], v214 offset:26624
	ds_read_b128 v[32:35], v214 offset:27648
	s_nop 7
	v_fma_f32 v234, |v36|, v253, v20
	v_fma_f32 v235, |v37|, v253, v21
	v_fma_f32 v236, |v38|, v253, v22
	v_fma_f32 v237, |v39|, v253, v23
	v_fma_f32 v40, |v40|, v253, v24
	v_fma_f32 v41, |v41|, v253, v25
	v_fma_f32 v42, |v42|, v253, v26
	v_fma_f32 v43, |v43|, v253, v27
	s_waitcnt lgkmcnt(3)
	v_mfma_f32_32x32x16_bf16 v[12:27], v[80:83], v[4:7], 0
	v_fma_f32 v44, |v44|, v253, v229
	v_fma_f32 v45, |v45|, v253, v230
	s_waitcnt lgkmcnt(2)
	v_mfma_f32_32x32x16_bf16 v[12:27], v[76:79], v[8:11], v[12:27]
	v_fma_f32 v46, |v46|, v253, v212
	v_fma_f32 v47, |v47|, v253, v213
	s_waitcnt lgkmcnt(1)
	v_mfma_f32_32x32x16_bf16 v[12:27], v[72:75], v[28:31], v[12:27]
	v_fma_f32 v48, |v48|, v253, v215
	v_fma_f32 v49, |v49|, v253, v216
	v_fma_f32 v50, |v50|, v253, v217
	v_fma_f32 v51, |v51|, v253, v228
	s_waitcnt lgkmcnt(0)
	v_mfma_f32_32x32x16_bf16 v[12:27], v[52:55], v[32:35], v[12:27]
	ds_read_b128 v[4:7], v214 offset:28672
	ds_read_b128 v[28:31], v214 offset:29696
	ds_read_b128 v[32:35], v214 offset:30720
	ds_read_b128 v[36:39], v214 offset:31744
	s_nop 7
	v_fma_f32 v212, |v12|, v223, v234
	v_fma_f32 v213, |v13|, v223, v235
	v_fma_f32 v215, |v14|, v223, v236
	v_fma_f32 v216, |v15|, v223, v237
	v_fma_f32 v217, |v16|, v223, v40
	v_fma_f32 v228, |v17|, v223, v41
	v_fma_f32 v229, |v18|, v223, v42
	v_fma_f32 v230, |v19|, v223, v43
	s_waitcnt lgkmcnt(3)
	v_mfma_f32_32x32x16_bf16 v[4:19], v[80:83], v[4:7], 0
	v_fma_f32 v234, |v20|, v223, v44
	v_fma_f32 v235, |v21|, v223, v45
	s_waitcnt lgkmcnt(2)
	v_mfma_f32_32x32x16_bf16 v[4:19], v[76:79], v[28:31], v[4:19]
	v_fma_f32 v236, |v22|, v223, v46
	v_fma_f32 v237, |v23|, v223, v47
	s_waitcnt lgkmcnt(1)
	v_mfma_f32_32x32x16_bf16 v[4:19], v[72:75], v[32:35], v[4:19]
	v_fma_f32 v48, |v24|, v223, v48
	v_fma_f32 v49, |v25|, v223, v49
	v_fma_f32 v50, |v26|, v223, v50
	v_fma_f32 v51, |v27|, v223, v51
	s_waitcnt lgkmcnt(0)
	v_mfma_f32_32x32x16_bf16 v[4:19], v[52:55], v[36:39], v[4:19]
	ds_read_b128 v[20:23], v214 offset:32768
	ds_read_b128 v[36:39], v214 offset:33792
	ds_read_b128 v[40:43], v214 offset:34816
	ds_read_b128 v[44:47], v214 offset:35840
	s_waitcnt lgkmcnt(3)
	v_mfma_f32_32x32x16_bf16 v[20:35], v[80:83], v[20:23], 0
	s_nop 5
	v_fma_f32 v212, |v4|, v219, v212
	v_fma_f32 v213, |v5|, v219, v213
	v_fma_f32 v4, |v6|, v219, v215
	v_fma_f32 v5, |v7|, v219, v216
	s_waitcnt lgkmcnt(2)
	v_mfma_f32_32x32x16_bf16 v[20:35], v[76:79], v[36:39], v[20:35]
	v_fma_f32 v6, |v8|, v219, v217
	v_fma_f32 v7, |v9|, v219, v228
	v_fma_f32 v8, |v10|, v219, v229
	v_fma_f32 v9, |v11|, v219, v230
	s_waitcnt lgkmcnt(1)
	v_mfma_f32_32x32x16_bf16 v[20:35], v[72:75], v[40:43], v[20:35]
	v_fma_f32 v36, |v12|, v219, v234
	v_fma_f32 v37, |v13|, v219, v235
	v_fma_f32 v38, |v14|, v219, v236
	v_fma_f32 v39, |v15|, v219, v237
	s_waitcnt lgkmcnt(0)
	v_mfma_f32_32x32x16_bf16 v[20:35], v[52:55], v[44:47], v[20:35]
	v_fma_f32 v16, |v16|, v219, v48
	v_fma_f32 v17, |v17|, v219, v49
	s_nop 9
	v_add_f32_e32 v20, v212, v20
	v_pk_add_f32 v[14:15], v[4:5], v[22:23]
	v_pk_add_f32 v[4:5], v[32:33], v[16:17]
	v_cvt_f16_f32_e32 v16, v20
	v_fma_f32 v18, |v18|, v219, v50
	v_fma_f32 v19, |v19|, v219, v51
	v_add_f32_e32 v21, v213, v21
	v_add_f32_e32 v17, v34, v18
	v_add_f32_e32 v19, v35, v19
	v_bitop3_b32 v18, v16, s7, v16 bitop3:0xc
	v_or_b32_e32 v20, 0x8000, v16
	v_cmp_gt_i16_e32 vcc, 0, v16
	v_pk_add_f32 v[10:11], v[8:9], v[26:27]
	v_pk_add_f32 v[8:9], v[36:37], v[28:29]
	v_cndmask_b32_e32 v26, v20, v18, vcc
	v_cvt_f16_f32_e32 v29, v21
	v_cvt_f16_f32_e32 v18, v17
	v_cvt_f16_f32_e32 v17, v19
	v_pk_add_f32 v[12:13], v[6:7], v[24:25]
	v_pk_add_f32 v[6:7], v[38:39], v[30:31]
	v_bitop3_b32 v30, v29, s7, v29 bitop3:0xc
	v_or_b32_e32 v31, 0x8000, v29
	v_cmp_gt_i16_e64 s[60:61], 0, v29
	v_bitop3_b32 v21, v18, s7, v18 bitop3:0xc
	v_or_b32_e32 v22, 0x8000, v18
	v_cmp_gt_i16_e64 s[58:59], 0, v18
	v_bitop3_b32 v19, v17, s7, v17 bitop3:0xc
	v_or_b32_e32 v20, 0x8000, v17
	v_cmp_gt_i16_e32 vcc, 0, v17
	s_cbranch_scc1 .LBB0_384
	v_bfe_u32 v16, v26, 8, 8
	v_lshl_add_u32 v16, v16, 2, v222
	ds_add_u32 v16, v224 offset:36864
	v_cndmask_b32_e64 v16, v31, v30, s[60:61]
	v_cndmask_b32_e32 v40, v20, v19, vcc
	v_cndmask_b32_e64 v38, v22, v21, s[58:59]
	v_bfe_u32 v23, v16, 8, 8
	v_lshl_add_u32 v23, v23, 2, v222
	ds_add_u32 v23, v224 offset:36864
	v_lshrrev_b32_e32 v41, 8, v40
	v_bfe_u32 v24, v38, 8, 8
	v_lshl_add_u32 v24, v24, 2, v222
	ds_add_u32 v24, v224 offset:36864
	s_mov_b64 s[0:1], 0
	v_cvt_pk_f16_f32 v23, v6, v7
	v_pk_ashrrev_i16 v24, 15, v23 op_sel_hi:[0,1]
	v_bitop3_b32 v7, v23, v24, s32 bitop3:0x1e
	v_pk_lshrrev_b16 v23, 8, v7 op_sel_hi:[0,1]
	v_and_b32_e32 v24, 0xff, v23
	v_lshl_add_u32 v24, v24, 2, v222
	v_lshrrev_b32_e32 v23, 14, v23
	ds_add_u32 v24, v224 offset:36864
	v_add_u32_e32 v23, v222, v23
	ds_add_u32 v23, v224 offset:36864
	v_cvt_pk_f16_f32 v25, v8, v9
	v_pk_ashrrev_i16 v27, 15, v25 op_sel_hi:[0,1]
	v_bitop3_b32 v6, v25, v27, s32 bitop3:0x1e
	v_pk_lshrrev_b16 v25, 8, v6 op_sel_hi:[0,1]
	v_and_b32_e32 v27, 0xff, v25
	v_lshl_add_u32 v27, v27, 2, v222
	v_lshrrev_b32_e32 v25, 14, v25
	ds_add_u32 v27, v224 offset:36864
	v_add_u32_e32 v25, v222, v25
	ds_add_u32 v25, v224 offset:36864
	v_cvt_pk_f16_f32 v28, v10, v11
	v_pk_ashrrev_i16 v32, 15, v28 op_sel_hi:[0,1]
	v_bitop3_b32 v9, v28, v32, s32 bitop3:0x1e
	v_pk_lshrrev_b16 v28, 8, v9 op_sel_hi:[0,1]
	v_and_b32_e32 v32, 0xff, v28
	v_lshl_add_u32 v32, v32, 2, v222
	v_lshrrev_b32_e32 v28, 14, v28
	ds_add_u32 v32, v224 offset:36864
	v_add_u32_e32 v28, v222, v28
	ds_add_u32 v28, v224 offset:36864
	v_cvt_pk_f16_f32 v33, v12, v13
	v_pk_ashrrev_i16 v34, 15, v33 op_sel_hi:[0,1]
	v_bitop3_b32 v8, v33, v34, s32 bitop3:0x1e
	v_pk_lshrrev_b16 v33, 8, v8 op_sel_hi:[0,1]
	v_and_b32_e32 v34, 0xff, v33
	v_lshl_add_u32 v34, v34, 2, v222
	v_lshrrev_b32_e32 v33, 14, v33
	ds_add_u32 v34, v224 offset:36864
	v_add_u32_e32 v33, v222, v33
	ds_add_u32 v33, v224 offset:36864
	v_cvt_pk_f16_f32 v35, v4, v5
	v_pk_ashrrev_i16 v36, 15, v35 op_sel_hi:[0,1]
	v_bitop3_b32 v10, v35, v36, s32 bitop3:0x1e
	v_pk_lshrrev_b16 v35, 8, v10 op_sel_hi:[0,1]
	v_and_b32_e32 v36, 0xff, v35
	v_lshl_add_u32 v36, v36, 2, v222
	v_lshrrev_b32_e32 v35, 14, v35
	ds_add_u32 v36, v224 offset:36864
	v_add_u32_e32 v35, v222, v35
	ds_add_u32 v35, v224 offset:36864
	v_cvt_pk_f16_f32 v37, v14, v15
	v_pk_ashrrev_i16 v39, 15, v37 op_sel_hi:[0,1]
	v_bitop3_b32 v5, v37, v39, s32 bitop3:0x1e
	v_pk_lshrrev_b16 v37, 8, v5 op_sel_hi:[0,1]
	v_and_b32_e32 v39, 0xff, v37
	v_lshl_add_u32 v39, v39, 2, v222
	v_lshrrev_b32_e32 v37, 14, v37
	ds_add_u32 v39, v224 offset:36864
	v_add_u32_e32 v37, v222, v37
	ds_add_u32 v37, v224 offset:36864
	v_lshl_add_u32 v42, v41, 2, v222
	ds_add_u32 v42, v224 offset:36864
	v_lshl_or_b32 v4, v16, 16, v26
	v_lshl_or_b32 v11, v40, 16, v38
	s_nop 1
	s_branch .Lidx_join

.Lidx_join:
	v_permlane32_swap_b32_e32 v4, v6
	v_permlane32_swap_b32_e32 v5, v7
	v_permlane32_swap_b32_e32 v8, v10
	v_permlane32_swap_b32_e32 v9, v11
	s_andn2_b64 vcc, exec, s[82:83]
	global_store_dwordx4 v231, v[4:7], s[12:13]
	global_store_dwordx4 v231, v[8:11], s[12:13] offset:16
	s_cbranch_vccnz .LBB0_388
	s_waitcnt vmcnt(2)
	v_mov_b64_e32 v[52:53], v[56:57]
	v_mov_b64_e32 v[74:75], v[62:63]
	v_mov_b64_e32 v[78:79], v[66:67]
	v_mov_b64_e32 v[82:83], v[70:71]
	v_mov_b64_e32 v[54:55], v[58:59]
	v_mov_b64_e32 v[72:73], v[60:61]
	v_mov_b64_e32 v[76:77], v[64:65]
	v_mov_b64_e32 v[80:81], v[68:69]
